# combo17 + strategy 4 other half: one static s_setprio 1 for waves 0-3 over the attention phase
# baseline (speedup 1.0000x reference)
.LBB0_493:
	s_or_b64 exec, exec, s[24:25]
	s_mov_b32 s0, s61
	s_waitcnt lgkmcnt(0)
	s_barrier
	s_cmp_lt_u32 s61, 4
	s_cbranch_scc0 .Lprio_attn
	s_setprio 1
